# nt hint on the once-read f32 expert-weight loads of the conversion pool
# speedup vs baseline: 1.0131x; 1.0077x over previous
; #define LAS __attribute__((address_space(3)))
; DI int lane_id() { int l; asm volatile("v_mbcnt_lo_u32_b32 %0, -1, 0\n\tv_mbcnt_hi_u32_b32 %0, -1, %0" : "=v"(l)); return l; }
; DI int wave_in_wg() { return __builtin_amdgcn_readfirstlane(((const LAS int*)((LAS unsigned char*)lds_raw + LDS_CTL_OFF + 1024))[hw_wave_slot()]); }
; DI CvItem cv_decode(const Params& P, int it) { CvItem c; int item;
;     if (it < NE * CV_GU1) { const int e = it / CV_GU1; c.W = P.in[I_WGU] + (size_t)e * D * 4096; c.N = 4096; c.WT = (unsigned char*)(P.ws + WS_WGU) + (size_t)e * 4096 * D; c.kind = 2; item = it % CV_GU1; }
;     else { const int r = it - NE * CV_GU1; const int e = r / CV_DN1; c.W = P.in[I_WDN] + (size_t)e * D * D; c.N = D; c.WT = (unsigned char*)(P.ws + WS_WDN) + (size_t)e * D * D; c.kind = 3; item = r % CV_DN1; }
;     const int nblk = c.N / 32, kb = item / nblk, nb = item % nblk; c.k0 = 128 * kb; c.n0 = 32 * nb; return c; }
; DI void cv_issue(const CvItem& c, int lane, f32x4 (&v)[16]) { const int c4 = (lane & 7) * 4, r8 = lane >> 3;
; #pragma unroll
;     for (int i = 0; i < 16; ++i) v[i] = *(const f32x4*)(c.W + (size_t)(c.k0 + 8 * i + r8) * c.N + c.n0 + c4); }
; DI void conv_pool(const Params& P, LAS unsigned char* lds, int pool, int blk_lo, int blk_hi) {
;     const int wid = wave_in_wg(), lane = lane_id();
;     LAS float* scr = (LAS float*)(lds + wid * 16896);
;     unsigned* ctr = (unsigned*)(P.ws + WS_CTL) + CW_POOL + pool * 64;
;     const int CV_NBLK = blk_hi;
;     auto claim = [&]() -> int { unsigned v_ = 0u; if (lane == 0) v_ = __hip_atomic_fetch_add(ctr, 1u, __ATOMIC_RELAXED, __HIP_MEMORY_SCOPE_AGENT); return blk_lo + (int)__builtin_amdgcn_readfirstlane(v_); };
;     const int blk = claim(); if (blk >= CV_NBLK) return;
;     int it = blk * CV_BLK, left = CV_BLK;
;     CvItem cur = cv_decode(P, it); f32x4 v[16]; cv_issue(cur, lane, v);
.LBB0_368:
	s_lshr_b32 s13, s16, 5
	s_sext_i32_i16 s2, s10
	v_cvt_f32_ubyte0_e32 v1, s13
	v_cvt_f32_i32_e32 v0, s2
	v_rcp_iflag_f32_e32 v2, v1
	s_mulk_i32 s12, 0x4200
	s_ashr_i32 s2, s2, 30
	s_add_i32 s33, s12, 0
	v_mul_f32_e32 v2, v0, v2
	v_trunc_f32_e32 v2, v2
	v_fma_f32 v0, -v2, v1, v0
	v_cvt_i32_f32_e32 v2, v2
	s_or_b32 s12, s2, 1
	v_cmp_ge_f32_e64 s[2:3], |v0|, v1
	s_and_b64 s[2:3], s[2:3], exec
	s_cselect_b32 s2, s12, 0
	v_readfirstlane_b32 s3, v2
	s_add_i32 s2, s3, s2
	s_sext_i32_i16 s3, s2
	s_mul_i32 s2, s2, s13
	s_sub_i32 s2, s10, s2
	v_ashrrev_i32_e32 v132, 3, v56
	s_sext_i32_i16 s2, s2
	s_lshl_b32 s10, s3, 7
	v_lshlrev_b32_e32 v0, 2, v56
	v_add_u32_e32 v133, 8, v132
	v_add_u32_e32 v134, 16, v132
	v_add_u32_e32 v135, 24, v132
	v_add_u32_e32 v136, 32, v132
	v_add_u32_e32 v137, 40, v132
	v_add_u32_e32 v138, 48, v132
	v_add_u32_e32 v139, 56, v132
	v_add_u32_e32 v140, 64, v132
	v_add_u32_e32 v141, 0x48, v132
	v_add_u32_e32 v142, 0x50, v132
	v_add_u32_e32 v143, 0x58, v132
	v_add_u32_e32 v144, 0x60, v132
	v_add_u32_e32 v145, 0x68, v132
	v_add_u32_e32 v146, 0x70, v132
	s_lshl_b32 s12, s2, 5
	v_and_b32_e32 v58, 28, v0
	v_add_u32_e32 v0, s10, v132
	v_add_u32_e32 v2, s10, v133
	v_add_u32_e32 v8, s10, v134
	v_add_u32_e32 v10, s10, v135
	v_add_u32_e32 v16, s10, v136
	v_add_u32_e32 v18, s10, v137
	v_add_u32_e32 v24, s10, v138
	v_add_u32_e32 v26, s10, v139
	v_add_u32_e32 v32, s10, v140
	v_add_u32_e32 v34, s10, v141
	v_add_u32_e32 v40, s10, v142
	v_add_u32_e32 v42, s10, v143
	v_add_u32_e32 v48, s10, v144
	v_add_u32_e32 v50, s10, v145
	v_add_u32_e32 v57, s10, v146
	v_add_u32_e32 v147, 0x78, v132
	v_mad_i64_i32 v[0:1], s[2:3], v0, s16, 0
	s_ashr_i32 s13, s12, 31
	v_mad_i64_i32 v[2:3], s[22:23], v2, s16, 0
	v_mad_i64_i32 v[8:9], s[22:23], v8, s16, 0
	v_mad_i64_i32 v[10:11], s[22:23], v10, s16, 0
	v_mad_i64_i32 v[16:17], s[22:23], v16, s16, 0
	v_mad_i64_i32 v[18:19], s[22:23], v18, s16, 0
	v_mad_i64_i32 v[24:25], s[22:23], v24, s16, 0
	v_mad_i64_i32 v[26:27], s[22:23], v26, s16, 0
	v_mad_i64_i32 v[32:33], s[22:23], v32, s16, 0
	v_mad_i64_i32 v[34:35], s[22:23], v34, s16, 0
	v_mad_i64_i32 v[40:41], s[22:23], v40, s16, 0
	v_mad_i64_i32 v[42:43], s[22:23], v42, s16, 0
	v_mad_i64_i32 v[48:49], s[22:23], v48, s16, 0
	v_mad_i64_i32 v[50:51], s[22:23], v50, s16, 0
	v_mad_i64_i32 v[60:61], s[22:23], v57, s16, 0
	v_add_u32_e32 v57, s10, v147
	v_lshl_add_u64 v[0:1], v[0:1], 2, s[14:15]
	s_lshl_b64 s[2:3], s[12:13], 2
	v_lshl_add_u64 v[2:3], v[2:3], 2, s[14:15]
	v_lshl_add_u64 v[8:9], v[8:9], 2, s[14:15]
	v_lshl_add_u64 v[10:11], v[10:11], 2, s[14:15]
	v_lshl_add_u64 v[16:17], v[16:17], 2, s[14:15]
	v_lshl_add_u64 v[18:19], v[18:19], 2, s[14:15]
	v_lshl_add_u64 v[24:25], v[24:25], 2, s[14:15]
	v_lshl_add_u64 v[26:27], v[26:27], 2, s[14:15]
	v_lshl_add_u64 v[32:33], v[32:33], 2, s[14:15]
	v_lshl_add_u64 v[34:35], v[34:35], 2, s[14:15]
	v_lshl_add_u64 v[40:41], v[40:41], 2, s[14:15]
	v_lshl_add_u64 v[42:43], v[42:43], 2, s[14:15]
	v_lshl_add_u64 v[48:49], v[48:49], 2, s[14:15]
	v_lshl_add_u64 v[50:51], v[50:51], 2, s[14:15]
	v_lshl_add_u64 v[60:61], v[60:61], 2, s[14:15]
	v_mad_i64_i32 v[62:63], s[16:17], v57, s16, 0
	v_mov_b32_e32 v129, 0
	v_lshl_add_u64 v[0:1], v[0:1], 0, s[2:3]
	v_lshlrev_b32_e32 v128, 2, v58
	v_lshl_add_u64 v[2:3], v[2:3], 0, s[2:3]
	v_lshl_add_u64 v[8:9], v[8:9], 0, s[2:3]
	v_lshl_add_u64 v[10:11], v[10:11], 0, s[2:3]
	v_lshl_add_u64 v[16:17], v[16:17], 0, s[2:3]
	v_lshl_add_u64 v[18:19], v[18:19], 0, s[2:3]
	v_lshl_add_u64 v[24:25], v[24:25], 0, s[2:3]
	v_lshl_add_u64 v[26:27], v[26:27], 0, s[2:3]
	v_lshl_add_u64 v[32:33], v[32:33], 0, s[2:3]
	v_lshl_add_u64 v[34:35], v[34:35], 0, s[2:3]
	v_lshl_add_u64 v[40:41], v[40:41], 0, s[2:3]
	v_lshl_add_u64 v[42:43], v[42:43], 0, s[2:3]
	v_lshl_add_u64 v[48:49], v[48:49], 0, s[2:3]
	v_lshl_add_u64 v[50:51], v[50:51], 0, s[2:3]
	v_lshl_add_u64 v[60:61], v[60:61], 0, s[2:3]
	v_lshl_add_u64 v[62:63], v[62:63], 2, s[14:15]
	v_lshl_add_u64 v[0:1], v[0:1], 0, v[128:129]
	v_lshl_add_u64 v[2:3], v[2:3], 0, v[128:129]
	v_lshl_add_u64 v[8:9], v[8:9], 0, v[128:129]
	v_lshl_add_u64 v[10:11], v[10:11], 0, v[128:129]
	v_lshl_add_u64 v[16:17], v[16:17], 0, v[128:129]
	v_lshl_add_u64 v[18:19], v[18:19], 0, v[128:129]
	v_lshl_add_u64 v[24:25], v[24:25], 0, v[128:129]
	v_lshl_add_u64 v[26:27], v[26:27], 0, v[128:129]
	v_lshl_add_u64 v[32:33], v[32:33], 0, v[128:129]
	v_lshl_add_u64 v[34:35], v[34:35], 0, v[128:129]
	v_lshl_add_u64 v[40:41], v[40:41], 0, v[128:129]
	v_lshl_add_u64 v[42:43], v[42:43], 0, v[128:129]
	v_lshl_add_u64 v[48:49], v[48:49], 0, v[128:129]
	v_lshl_add_u64 v[50:51], v[50:51], 0, v[128:129]
	v_lshl_add_u64 v[60:61], v[60:61], 0, v[128:129]
	v_lshl_add_u64 v[62:63], v[62:63], 0, s[2:3]
	global_load_dwordx4 v[4:7], v[0:1], off nt
	s_nop 0
	global_load_dwordx4 v[0:3], v[2:3], off nt
	s_nop 0
	global_load_dwordx4 v[12:15], v[8:9], off nt
	s_nop 0
	global_load_dwordx4 v[8:11], v[10:11], off nt
	s_nop 0
	global_load_dwordx4 v[20:23], v[16:17], off nt
	s_nop 0
	global_load_dwordx4 v[16:19], v[18:19], off nt
	s_nop 0
	global_load_dwordx4 v[28:31], v[24:25], off nt
	s_nop 0
	global_load_dwordx4 v[24:27], v[26:27], off nt
	s_nop 0
	global_load_dwordx4 v[36:39], v[32:33], off nt
	s_nop 0
	global_load_dwordx4 v[32:35], v[34:35], off nt
	s_nop 0
	global_load_dwordx4 v[44:47], v[40:41], off nt
	s_nop 0
	global_load_dwordx4 v[40:43], v[42:43], off nt
	s_nop 0
	global_load_dwordx4 v[52:55], v[48:49], off nt
	s_nop 0
	global_load_dwordx4 v[48:51], v[50:51], off nt
	v_lshl_add_u64 v[62:63], v[62:63], 0, v[128:129]
	global_load_dwordx4 v[68:71], v[60:61], off nt
	global_load_dwordx4 v[64:67], v[62:63], off nt
	v_readlane_b32 s40, v254, 2
	v_and_b32_e32 v56, 7, v56
	v_readlane_b32 s42, v254, 4
	v_lshlrev_b32_e32 v130, 4, v56
	v_mul_u32_u24_e32 v56, 0x840, v56
	v_lshlrev_b32_e32 v60, 2, v132
	v_readlane_b32 s43, v254, 5
	s_add_u32 s13, s42, 0x12400000
	v_add_u32_e32 v57, s33, v130
	s_movk_i32 s2, 0x84
	v_add3_u32 v148, s33, v56, v60
	s_addc_u32 s33, s43, 0
	v_mul_lo_u32 v59, v132, s2
	s_add_u32 s34, s42, 0x2400000
	s_mov_b32 s15, 0
	s_mov_b32 s14, 8
	v_mov_b32_e32 v131, v129
	s_addc_u32 s35, s43, 0
	v_lshlrev_b32_e32 v128, 2, v58
	v_add_u32_e32 v149, v57, v59
	s_movk_i32 s42, 0x7f
	v_readlane_b32 s41, v254, 3
	s_branch .LBB0_371

; #define LAS __attribute__((address_space(3)))
; DI CvItem cv_decode(const Params& P, int it) { CvItem c; int item;
;     if (it < NE * CV_GU1) { const int e = it / CV_GU1; c.W = P.in[I_WGU] + (size_t)e * D * 4096; c.N = 4096; c.WT = (unsigned char*)(P.ws + WS_WGU) + (size_t)e * 4096 * D; c.kind = 2; item = it % CV_GU1; }
;     else { const int r = it - NE * CV_GU1; const int e = r / CV_DN1; c.W = P.in[I_WDN] + (size_t)e * D * D; c.N = D; c.WT = (unsigned char*)(P.ws + WS_WDN) + (size_t)e * D * D; c.kind = 3; item = r % CV_DN1; }
;     const int nblk = c.N / 32, kb = item / nblk, nb = item % nblk; c.k0 = 128 * kb; c.n0 = 32 * nb; return c; }
; DI void cv_issue(const CvItem& c, int lane, f32x4 (&v)[16]) { const int c4 = (lane & 7) * 4, r8 = lane >> 3;
; #pragma unroll
;     for (int i = 0; i < 16; ++i) v[i] = *(const f32x4*)(c.W + (size_t)(c.k0 + 8 * i + r8) * c.N + c.n0 + c4); }
; DI void cv_finish(const CvItem& cc, int lane, LAS float* scr, const f32x4 (&v)[16]) {
;     { const int c4 = (lane & 7) * 4, r8 = lane >> 3;
; #pragma unroll
;       for (int i = 0; i < 16; ++i) { LAS float* d = scr + (8 * i + r8) * 33 + c4; d[0] = v[i][0]; d[1] = v[i][1]; d[2] = v[i][2]; d[3] = v[i][3]; } }
.LBB0_370:
	s_lshr_b32 s39, s48, 5
	s_sext_i32_i16 s2, s38
	v_cvt_f32_ubyte0_e32 v57, s39
	v_cvt_f32_i32_e32 v56, s2
	v_rcp_iflag_f32_e32 v58, v57
	s_ashr_i32 s2, s2, 30
	s_or_b32 s45, s2, 1
	v_mul_f32_e32 v58, v56, v58
	v_trunc_f32_e32 v58, v58
	v_fma_f32 v56, -v58, v57, v56
	v_cvt_i32_f32_e32 v58, v58
	v_cmp_ge_f32_e64 s[2:3], |v56|, v57
	s_and_b64 s[2:3], s[2:3], exec
	s_cselect_b32 s2, s45, 0
	v_readfirstlane_b32 s3, v58
	s_add_i32 s2, s3, s2
	s_sext_i32_i16 s3, s2
	s_mul_i32 s2, s2, s39
	s_sub_i32 s2, s38, s2
	s_sext_i32_i16 s2, s2
	s_lshl_b32 s45, s3, 7
	s_lshl_b32 s38, s2, 5
	v_add_u32_e32 v56, s45, v132
	v_add_u32_e32 v58, s45, v133
	s_waitcnt vmcnt(19)
	v_add_u32_e32 v72, s45, v134
	v_add_u32_e32 v74, s45, v135
	v_add_u32_e32 v80, s45, v136
	v_add_u32_e32 v82, s45, v137
	v_add_u32_e32 v88, s45, v138
	v_add_u32_e32 v90, s45, v139
	v_add_u32_e32 v96, s45, v140
	v_add_u32_e32 v98, s45, v141
	v_add_u32_e32 v104, s45, v142
	v_add_u32_e32 v106, s45, v143
	v_add_u32_e32 v112, s45, v144
	v_add_u32_e32 v114, s45, v145
	v_add_u32_e32 v120, s45, v146
	v_add_u32_e32 v122, s45, v147
	v_mad_i64_i32 v[56:57], s[2:3], v56, s48, 0
	s_ashr_i32 s39, s38, 31
	v_mad_i64_i32 v[58:59], s[50:51], v58, s48, 0
	v_mad_i64_i32 v[72:73], s[50:51], v72, s48, 0
	v_mad_i64_i32 v[74:75], s[50:51], v74, s48, 0
	v_mad_i64_i32 v[80:81], s[50:51], v80, s48, 0
	v_mad_i64_i32 v[82:83], s[50:51], v82, s48, 0
	v_mad_i64_i32 v[88:89], s[50:51], v88, s48, 0
	v_mad_i64_i32 v[90:91], s[50:51], v90, s48, 0
	v_mad_i64_i32 v[96:97], s[50:51], v96, s48, 0
	v_mad_i64_i32 v[98:99], s[50:51], v98, s48, 0
	v_mad_i64_i32 v[104:105], s[50:51], v104, s48, 0
	v_mad_i64_i32 v[106:107], s[50:51], v106, s48, 0
	v_mad_i64_i32 v[112:113], s[50:51], v112, s48, 0
	v_mad_i64_i32 v[114:115], s[50:51], v114, s48, 0
	v_mad_i64_i32 v[120:121], s[50:51], v120, s48, 0
	v_mad_i64_i32 v[122:123], s[48:49], v122, s48, 0
	v_lshl_add_u64 v[56:57], v[56:57], 2, s[40:41]
	s_lshl_b64 s[2:3], s[38:39], 2
	v_lshl_add_u64 v[58:59], v[58:59], 2, s[40:41]
	v_lshl_add_u64 v[72:73], v[72:73], 2, s[40:41]
	v_lshl_add_u64 v[74:75], v[74:75], 2, s[40:41]
	v_lshl_add_u64 v[80:81], v[80:81], 2, s[40:41]
	v_lshl_add_u64 v[82:83], v[82:83], 2, s[40:41]
	v_lshl_add_u64 v[88:89], v[88:89], 2, s[40:41]
	v_lshl_add_u64 v[90:91], v[90:91], 2, s[40:41]
	v_lshl_add_u64 v[96:97], v[96:97], 2, s[40:41]
	v_lshl_add_u64 v[98:99], v[98:99], 2, s[40:41]
	v_lshl_add_u64 v[104:105], v[104:105], 2, s[40:41]
	v_lshl_add_u64 v[106:107], v[106:107], 2, s[40:41]
	v_lshl_add_u64 v[112:113], v[112:113], 2, s[40:41]
	v_lshl_add_u64 v[114:115], v[114:115], 2, s[40:41]
	v_lshl_add_u64 v[120:121], v[120:121], 2, s[40:41]
	v_lshl_add_u64 v[122:123], v[122:123], 2, s[40:41]
	v_lshl_add_u64 v[56:57], v[56:57], 0, s[2:3]
	v_lshl_add_u64 v[58:59], v[58:59], 0, s[2:3]
	v_lshl_add_u64 v[72:73], v[72:73], 0, s[2:3]
	v_lshl_add_u64 v[74:75], v[74:75], 0, s[2:3]
	v_lshl_add_u64 v[80:81], v[80:81], 0, s[2:3]
	v_lshl_add_u64 v[82:83], v[82:83], 0, s[2:3]
	v_lshl_add_u64 v[88:89], v[88:89], 0, s[2:3]
	v_lshl_add_u64 v[90:91], v[90:91], 0, s[2:3]
	v_lshl_add_u64 v[96:97], v[96:97], 0, s[2:3]
	v_lshl_add_u64 v[98:99], v[98:99], 0, s[2:3]
	v_lshl_add_u64 v[104:105], v[104:105], 0, s[2:3]
	v_lshl_add_u64 v[106:107], v[106:107], 0, s[2:3]
	v_lshl_add_u64 v[112:113], v[112:113], 0, s[2:3]
	v_lshl_add_u64 v[114:115], v[114:115], 0, s[2:3]
	v_lshl_add_u64 v[120:121], v[120:121], 0, s[2:3]
	v_lshl_add_u64 v[122:123], v[122:123], 0, s[2:3]
	v_lshl_add_u64 v[56:57], v[56:57], 0, v[128:129]
	v_lshl_add_u64 v[60:61], v[58:59], 0, v[128:129]
	v_lshl_add_u64 v[72:73], v[72:73], 0, v[128:129]
	s_waitcnt vmcnt(17)
	v_lshl_add_u64 v[76:77], v[74:75], 0, v[128:129]
	v_lshl_add_u64 v[80:81], v[80:81], 0, v[128:129]
	v_lshl_add_u64 v[84:85], v[82:83], 0, v[128:129]
	v_lshl_add_u64 v[88:89], v[88:89], 0, v[128:129]
	v_lshl_add_u64 v[92:93], v[90:91], 0, v[128:129]
	v_lshl_add_u64 v[96:97], v[96:97], 0, v[128:129]
	v_lshl_add_u64 v[100:101], v[98:99], 0, v[128:129]
	v_lshl_add_u64 v[104:105], v[104:105], 0, v[128:129]
	v_lshl_add_u64 v[108:109], v[106:107], 0, v[128:129]
	v_lshl_add_u64 v[112:113], v[112:113], 0, v[128:129]
	v_lshl_add_u64 v[116:117], v[114:115], 0, v[128:129]
	v_lshl_add_u64 v[120:121], v[120:121], 0, v[128:129]
	v_lshl_add_u64 v[124:125], v[122:123], 0, v[128:129]
	global_load_dwordx4 v[56:59], v[56:57], off nt
	s_nop 0
	global_load_dwordx4 v[60:63], v[60:61], off nt
	s_nop 0
	global_load_dwordx4 v[72:75], v[72:73], off nt
	s_nop 0
	global_load_dwordx4 v[76:79], v[76:77], off nt
	s_nop 0
	global_load_dwordx4 v[80:83], v[80:81], off nt
	s_nop 0
	global_load_dwordx4 v[84:87], v[84:85], off nt
	s_nop 0
	global_load_dwordx4 v[88:91], v[88:89], off nt
	s_nop 0
	global_load_dwordx4 v[92:95], v[92:93], off nt
	s_nop 0
	global_load_dwordx4 v[96:99], v[96:97], off nt
	s_nop 0
	global_load_dwordx4 v[100:103], v[100:101], off nt
	s_nop 0
	global_load_dwordx4 v[104:107], v[104:105], off nt
	s_nop 0
	global_load_dwordx4 v[108:111], v[108:109], off nt
	s_nop 0
	global_load_dwordx4 v[112:115], v[112:113], off nt
	s_nop 0
	global_load_dwordx4 v[116:119], v[116:117], off nt
	s_nop 0
	global_load_dwordx4 v[120:123], v[120:121], off nt
	s_nop 0
	global_load_dwordx4 v[124:127], v[124:125], off nt
	s_waitcnt vmcnt(31)
	ds_write2_b32 v149, v4, v5 offset1:1
	ds_write2_b32 v149, v6, v7 offset0:2 offset1:3
	v_add_u32_e32 v4, 0x420, v149
	s_waitcnt vmcnt(30)
	ds_write2_b32 v4, v0, v1 offset1:1
	v_add_u32_e32 v0, 0x428, v149
	ds_write2_b32 v0, v2, v3 offset1:1
	v_add_u32_e32 v0, 0x840, v149
	s_waitcnt vmcnt(29)
; #define LAS __attribute__((address_space(3)))
; DI unsigned pk4f8(float a, float b, float c, float d) { int p = __builtin_amdgcn_cvt_pk_fp8_f32(a, b, 0, false); p = __builtin_amdgcn_cvt_pk_fp8_f32(c, d, p, true); return (unsigned)p; }
; DI void cv_finish(const CvItem& cc, int lane, LAS float* scr, const f32x4 (&v)[16]) {
;     { const int c4 = (lane & 7) * 4, r8 = lane >> 3;
; #pragma unroll
;       for (int i = 0; i < 16; ++i) { LAS float* d = scr + (8 * i + r8) * 33 + c4; d[0] = v[i][0]; d[1] = v[i][1]; d[2] = v[i][2]; d[3] = v[i][3]; } }
;     asm volatile("s_waitcnt lgkmcnt(0)" ::: "memory");
;     const int c = lane & 7;
; #pragma unroll
;     for (int j = 0; j < 4; ++j) { const int n = (lane >> 3) + 8 * j; const int src = cc.n0 + n; int dst = src;
;         if (cc.kind == 2) { const int jj = src & 2047; dst = (jj >> 7) * 256 + (src >> 11) * 128 + (jj & 127); }
;         const LAS float* sp = scr + (16 * c) * 33 + n;
;         u32x4 o; o.x = pk4f8(sp[0 * 33] * WSCALE, sp[1 * 33] * WSCALE, sp[2 * 33] * WSCALE, sp[3 * 33] * WSCALE); o.y = pk4f8(sp[4 * 33] * WSCALE, sp[5 * 33] * WSCALE, sp[6 * 33] * WSCALE, sp[7 * 33] * WSCALE);
;         o.z = pk4f8(sp[8 * 33] * WSCALE, sp[9 * 33] * WSCALE, sp[10 * 33] * WSCALE, sp[11 * 33] * WSCALE); o.w = pk4f8(sp[12 * 33] * WSCALE, sp[13 * 33] * WSCALE, sp[14 * 33] * WSCALE, sp[15 * 33] * WSCALE);
;         *(u32x4*)(cc.WT + (size_t)dst * D + cc.k0 + 16 * c) = o; }
	ds_write2_b32 v0, v12, v13 offset1:1
	v_add_u32_e32 v0, 0x848, v149
	ds_write2_b32 v0, v14, v15 offset1:1
	v_add_u32_e32 v0, 0xc60, v149
	s_waitcnt vmcnt(28)
	ds_write2_b32 v0, v8, v9 offset1:1
	v_add_u32_e32 v0, 0xc68, v149
	ds_write2_b32 v0, v10, v11 offset1:1
	v_add_u32_e32 v0, 0x1080, v149
	s_waitcnt vmcnt(27)
	ds_write2_b32 v0, v20, v21 offset1:1
	v_add_u32_e32 v0, 0x1088, v149
	ds_write2_b32 v0, v22, v23 offset1:1
	v_add_u32_e32 v0, 0x14a0, v149
	s_waitcnt vmcnt(26)
	ds_write2_b32 v0, v16, v17 offset1:1
	v_add_u32_e32 v0, 0x14a8, v149
	ds_write2_b32 v0, v18, v19 offset1:1
	v_add_u32_e32 v0, 0x18c0, v149
	s_waitcnt vmcnt(25)
	ds_write2_b32 v0, v28, v29 offset1:1
	v_add_u32_e32 v0, 0x18c8, v149
	ds_write2_b32 v0, v30, v31 offset1:1
	v_add_u32_e32 v0, 0x1ce0, v149
	s_waitcnt vmcnt(24)
	ds_write2_b32 v0, v24, v25 offset1:1
	v_add_u32_e32 v0, 0x1ce8, v149
	ds_write2_b32 v0, v26, v27 offset1:1
	v_add_u32_e32 v0, 0x2100, v149
	s_waitcnt vmcnt(23)
	ds_write2_b32 v0, v36, v37 offset1:1
	v_add_u32_e32 v0, 0x2108, v149
	ds_write2_b32 v0, v38, v39 offset1:1
	v_add_u32_e32 v0, 0x2520, v149
	s_waitcnt vmcnt(22)
	ds_write2_b32 v0, v32, v33 offset1:1
	v_add_u32_e32 v0, 0x2528, v149
	ds_write2_b32 v0, v34, v35 offset1:1
	v_add_u32_e32 v0, 0x2940, v149
	s_waitcnt vmcnt(21)
	ds_write2_b32 v0, v44, v45 offset1:1
	v_add_u32_e32 v0, 0x2948, v149
	ds_write2_b32 v0, v46, v47 offset1:1
	v_add_u32_e32 v0, 0x2d60, v149
	s_waitcnt vmcnt(20)
	ds_write2_b32 v0, v40, v41 offset1:1
	v_add_u32_e32 v0, 0x2d68, v149
	ds_write2_b32 v0, v42, v43 offset1:1
	v_add_u32_e32 v0, 0x3180, v149
	s_waitcnt vmcnt(19)
	ds_write2_b32 v0, v52, v53 offset1:1
	v_add_u32_e32 v0, 0x3188, v149
	ds_write2_b32 v0, v54, v55 offset1:1
	v_add_u32_e32 v0, 0x35a0, v149
	s_waitcnt vmcnt(18)
	ds_write2_b32 v0, v48, v49 offset1:1
	v_add_u32_e32 v0, 0x35a8, v149
	ds_write2_b32 v0, v50, v51 offset1:1
	v_add_u32_e32 v0, 0x39c0, v149
	s_waitcnt vmcnt(17)
	ds_write2_b32 v0, v68, v69 offset1:1
	v_add_u32_e32 v0, 0x39c8, v149
	ds_write2_b32 v0, v70, v71 offset1:1
	v_add_u32_e32 v0, 0x3de0, v149
	s_waitcnt vmcnt(16)
	ds_write2_b32 v0, v64, v65 offset1:1
	v_add_u32_e32 v0, 0x3de8, v149
	ds_write2_b32 v0, v66, v67 offset1:1
	s_waitcnt lgkmcnt(0)
	v_add_u32_e32 v0, s12, v132
	v_lshlrev_b32_e32 v1, 1, v0
	v_ashrrev_i32_e32 v2, 4, v0
	ds_read2_b32 v[4:5], v148 offset1:8
	ds_read2_b32 v[6:7], v148 offset0:33 offset1:41
	ds_read2_b32 v[8:9], v148 offset0:66 offset1:74
	v_and_b32_e32 v1, 0xf00, v1
	v_and_b32_e32 v2, 0xffffff80, v2
	s_cmp_eq_u32 s11, 2
	v_add_u32_e32 v1, v1, v2
	v_and_or_b32 v1, v0, s42, v1
	s_cselect_b64 vcc, -1, 0
	ds_read2_b32 v[12:13], v148 offset0:99 offset1:107
	v_cndmask_b32_e32 v10, v0, v1, vcc
	s_waitcnt lgkmcnt(3)
	v_mul_f32_e32 v1, 0x44000000, v4
	s_waitcnt lgkmcnt(2)
	v_mul_f32_e32 v2, 0x44000000, v6
	v_mov_b32_e32 v0, v129
	v_cvt_pk_fp8_f32 v0, v1, v2
	ds_read2_b32 v[14:15], v148 offset0:132 offset1:140
	ds_read2_b32 v[16:17], v148 offset0:165 offset1:173
	ds_read2_b32 v[18:19], v148 offset0:198 offset1:206
	s_waitcnt lgkmcnt(4)
	v_mul_f32_e32 v3, 0x44000000, v8
	s_waitcnt lgkmcnt(3)
	v_mul_f32_e32 v1, 0x44000000, v12
	ds_read2_b32 v[20:21], v148 offset0:231 offset1:239
	v_add_u32_e32 v38, 0x400, v148
	v_cvt_pk_fp8_f32 v0, v3, v1 op_sel:[0,0,1]
	s_waitcnt lgkmcnt(3)
	v_mul_f32_e32 v2, 0x44000000, v14
	s_waitcnt lgkmcnt(2)
	v_mul_f32_e32 v3, 0x44000000, v16
	v_mov_b32_e32 v1, v129
	ds_read2_b32 v[22:23], v38 offset0:8 offset1:16
	v_cvt_pk_fp8_f32 v1, v2, v3
	ds_read2_b32 v[24:25], v38 offset0:41 offset1:49
	ds_read2_b32 v[26:27], v38 offset0:74 offset1:82
	ds_read2_b32 v[28:29], v38 offset0:107 offset1:115
	ds_read2_b32 v[30:31], v38 offset0:140 offset1:148
	ds_read2_b32 v[32:33], v38 offset0:173 offset1:181
	s_waitcnt lgkmcnt(7)
	v_mul_f32_e32 v4, 0x44000000, v18
	s_waitcnt lgkmcnt(6)
	v_mul_f32_e32 v2, 0x44000000, v20
	v_cvt_pk_fp8_f32 v1, v4, v2 op_sel:[0,0,1]
	s_waitcnt lgkmcnt(5)
	v_mul_f32_e32 v3, 0x44000000, v22
	s_waitcnt lgkmcnt(4)
	v_mul_f32_e32 v4, 0x44000000, v24
	v_mov_b32_e32 v2, v129
	ds_read2_b32 v[34:35], v38 offset0:206 offset1:214
	ds_read2_b32 v[36:37], v38 offset0:239 offset1:247
	v_cvt_pk_fp8_f32 v2, v3, v4
	s_waitcnt lgkmcnt(3)
	v_mul_f32_e32 v4, 0x44000000, v30
	s_waitcnt lgkmcnt(2)
	v_mul_f32_e32 v11, 0x44000000, v32
	v_mov_b32_e32 v3, v129
	v_cvt_pk_fp8_f32 v3, v4, v11
	v_mul_f32_e32 v6, 0x44000000, v26
	v_mul_f32_e32 v8, 0x44000000, v28
	v_cvt_pk_fp8_f32 v2, v6, v8 op_sel:[0,0,1]
	s_waitcnt lgkmcnt(1)
	v_mul_f32_e32 v4, 0x44000000, v34
	s_waitcnt lgkmcnt(0)
; #define LAS __attribute__((address_space(3)))
; DI unsigned pk4f8(float a, float b, float c, float d) { int p = __builtin_amdgcn_cvt_pk_fp8_f32(a, b, 0, false); p = __builtin_amdgcn_cvt_pk_fp8_f32(c, d, p, true); return (unsigned)p; }
; DI void cv_finish(const CvItem& cc, int lane, LAS float* scr, const f32x4 (&v)[16]) {
;     ...
;     const int c = lane & 7;
; #pragma unroll
;     for (int j = 0; j < 4; ++j) { const int n = (lane >> 3) + 8 * j; const int src = cc.n0 + n; int dst = src;
;         if (cc.kind == 2) { const int jj = src & 2047; dst = (jj >> 7) * 256 + (src >> 11) * 128 + (jj & 127); }
;         const LAS float* sp = scr + (16 * c) * 33 + n;
;         u32x4 o; o.x = pk4f8(sp[0 * 33] * WSCALE, sp[1 * 33] * WSCALE, sp[2 * 33] * WSCALE, sp[3 * 33] * WSCALE); o.y = pk4f8(sp[4 * 33] * WSCALE, sp[5 * 33] * WSCALE, sp[6 * 33] * WSCALE, sp[7 * 33] * WSCALE);
;         o.z = pk4f8(sp[8 * 33] * WSCALE, sp[9 * 33] * WSCALE, sp[10 * 33] * WSCALE, sp[11 * 33] * WSCALE); o.w = pk4f8(sp[12 * 33] * WSCALE, sp[13 * 33] * WSCALE, sp[14 * 33] * WSCALE, sp[15 * 33] * WSCALE);
;         *(u32x4*)(cc.WT + (size_t)dst * D + cc.k0 + 16 * c) = o; }
	v_mul_f32_e32 v6, 0x44000000, v36
	v_ashrrev_i32_e32 v11, 31, v10
	v_cvt_pk_fp8_f32 v3, v4, v6 op_sel:[0,0,1]
	v_lshlrev_b64 v[10:11], 11, v[10:11]
	v_lshl_add_u64 v[10:11], s[6:7], 0, v[10:11]
	s_ashr_i32 s11, s10, 31
	v_lshl_add_u64 v[10:11], v[10:11], 0, s[10:11]
	v_lshl_add_u64 v[10:11], v[10:11], 0, v[130:131]
	global_store_dwordx4 v[10:11], v[0:3], off
	v_mul_f32_e32 v6, 0x44000000, v17
	v_mul_f32_e32 v8, 0x44000000, v33
	v_add_u32_e32 v0, s12, v133
	v_lshlrev_b32_e32 v1, 1, v0
	v_ashrrev_i32_e32 v2, 4, v0
	v_and_b32_e32 v1, 0xf00, v1
	v_and_b32_e32 v2, 0xffffff80, v2
	v_add_u32_e32 v1, v1, v2
	v_and_or_b32 v1, v0, s42, v1
	v_cndmask_b32_e32 v4, v0, v1, vcc
	v_mul_f32_e32 v1, 0x44000000, v5
	v_mul_f32_e32 v2, 0x44000000, v7
	v_mov_b32_e32 v0, v129
	v_cvt_pk_fp8_f32 v0, v1, v2
	v_mul_f32_e32 v2, 0x44000000, v15
	v_mov_b32_e32 v1, v129
	v_cvt_pk_fp8_f32 v1, v2, v6
	v_mul_f32_e32 v3, 0x44000000, v9
	v_mul_f32_e32 v5, 0x44000000, v13
	v_cvt_pk_fp8_f32 v0, v3, v5 op_sel:[0,0,1]
	v_mul_f32_e32 v2, 0x44000000, v19
	v_mul_f32_e32 v3, 0x44000000, v21
	v_cvt_pk_fp8_f32 v1, v2, v3 op_sel:[0,0,1]
	v_mul_f32_e32 v3, 0x44000000, v23
	v_mul_f32_e32 v5, 0x44000000, v25
	v_mov_b32_e32 v2, v129
	v_cvt_pk_fp8_f32 v2, v3, v5
	v_mul_f32_e32 v5, 0x44000000, v31
	v_mov_b32_e32 v3, v129
	v_cvt_pk_fp8_f32 v3, v5, v8
	v_mul_f32_e32 v6, 0x44000000, v27
	v_mul_f32_e32 v7, 0x44000000, v29
	v_cvt_pk_fp8_f32 v2, v6, v7 op_sel:[0,0,1]
	v_mul_f32_e32 v5, 0x44000000, v35
	v_mul_f32_e32 v6, 0x44000000, v37
	v_cvt_pk_fp8_f32 v3, v5, v6 op_sel:[0,0,1]
	v_ashrrev_i32_e32 v5, 31, v4
	v_lshlrev_b64 v[4:5], 11, v[4:5]
	v_lshl_add_u64 v[4:5], s[6:7], 0, v[4:5]
	v_lshl_add_u64 v[4:5], v[4:5], 0, s[10:11]
	v_lshl_add_u64 v[4:5], v[4:5], 0, v[130:131]
	global_store_dwordx4 v[4:5], v[0:3], off
	ds_read2_b32 v[4:5], v148 offset0:16 offset1:24
	ds_read2_b32 v[6:7], v148 offset0:49 offset1:57
	ds_read2_b32 v[8:9], v148 offset0:82 offset1:90
	v_add_u32_e32 v0, s12, v134
	v_lshlrev_b32_e32 v1, 1, v0
	v_ashrrev_i32_e32 v2, 4, v0
	v_and_b32_e32 v1, 0xf00, v1
	v_and_b32_e32 v2, 0xffffff80, v2
	v_add_u32_e32 v1, v1, v2
	v_and_or_b32 v1, v0, s42, v1
	ds_read2_b32 v[12:13], v148 offset0:115 offset1:123
	v_cndmask_b32_e32 v10, v0, v1, vcc
	s_waitcnt lgkmcnt(3)
	v_mul_f32_e32 v1, 0x44000000, v4
	s_waitcnt lgkmcnt(2)
	v_mul_f32_e32 v2, 0x44000000, v6
	v_mov_b32_e32 v0, v129
	ds_read2_b32 v[14:15], v148 offset0:148 offset1:156
	ds_read2_b32 v[16:17], v148 offset0:181 offset1:189
	v_cvt_pk_fp8_f32 v0, v1, v2
	s_waitcnt lgkmcnt(3)
	v_mul_f32_e32 v3, 0x44000000, v8
	s_waitcnt lgkmcnt(2)
	v_mul_f32_e32 v1, 0x44000000, v12
	ds_read2_b32 v[18:19], v148 offset0:214 offset1:222
	ds_read2_b32 v[20:21], v148 offset0:247 offset1:255
	v_cvt_pk_fp8_f32 v0, v3, v1 op_sel:[0,0,1]
	s_waitcnt lgkmcnt(3)
	v_mul_f32_e32 v2, 0x44000000, v14
	s_waitcnt lgkmcnt(2)
	v_mul_f32_e32 v3, 0x44000000, v16
	v_mov_b32_e32 v1, v129
	ds_read2_b32 v[22:23], v38 offset0:24 offset1:32
	v_cvt_pk_fp8_f32 v1, v2, v3
	ds_read2_b32 v[24:25], v38 offset0:57 offset1:65
	ds_read2_b32 v[26:27], v38 offset0:90 offset1:98
	ds_read2_b32 v[28:29], v38 offset0:123 offset1:131
	ds_read2_b32 v[30:31], v38 offset0:156 offset1:164
	ds_read2_b32 v[32:33], v38 offset0:189 offset1:197
	s_waitcnt lgkmcnt(7)
	v_mul_f32_e32 v4, 0x44000000, v18
	s_waitcnt lgkmcnt(6)
	v_mul_f32_e32 v2, 0x44000000, v20
	v_cvt_pk_fp8_f32 v1, v4, v2 op_sel:[0,0,1]
	s_waitcnt lgkmcnt(5)
	v_mul_f32_e32 v3, 0x44000000, v22
	s_waitcnt lgkmcnt(4)
	v_mul_f32_e32 v4, 0x44000000, v24
	v_mov_b32_e32 v2, v129
	v_cvt_pk_fp8_f32 v2, v3, v4
	v_add_u32_e32 v3, 0x600, v148
	ds_read2_b32 v[34:35], v38 offset0:222 offset1:230
	ds_read2_b32 v[36:37], v3 offset0:127 offset1:135
	s_waitcnt lgkmcnt(3)
; #define LAS __attribute__((address_space(3)))
; DI unsigned pk4f8(float a, float b, float c, float d) { int p = __builtin_amdgcn_cvt_pk_fp8_f32(a, b, 0, false); p = __builtin_amdgcn_cvt_pk_fp8_f32(c, d, p, true); return (unsigned)p; }
; DI void cv_finish(const CvItem& cc, int lane, LAS float* scr, const f32x4 (&v)[16]) {
;     ...
;     for (int j = 0; j < 4; ++j) { const int n = (lane >> 3) + 8 * j; const int src = cc.n0 + n; int dst = src;
;         if (cc.kind == 2) { const int jj = src & 2047; dst = (jj >> 7) * 256 + (src >> 11) * 128 + (jj & 127); }
;         const LAS float* sp = scr + (16 * c) * 33 + n;
;         u32x4 o; o.x = pk4f8(sp[0 * 33] * WSCALE, sp[1 * 33] * WSCALE, sp[2 * 33] * WSCALE, sp[3 * 33] * WSCALE); o.y = pk4f8(sp[4 * 33] * WSCALE, sp[5 * 33] * WSCALE, sp[6 * 33] * WSCALE, sp[7 * 33] * WSCALE);
;         o.z = pk4f8(sp[8 * 33] * WSCALE, sp[9 * 33] * WSCALE, sp[10 * 33] * WSCALE, sp[11 * 33] * WSCALE); o.w = pk4f8(sp[12 * 33] * WSCALE, sp[13 * 33] * WSCALE, sp[14 * 33] * WSCALE, sp[15 * 33] * WSCALE);
;         *(u32x4*)(cc.WT + (size_t)dst * D + cc.k0 + 16 * c) = o; }
;     asm volatile("s_waitcnt lgkmcnt(0)" ::: "memory");
; DI void conv_pool(const Params& P, LAS unsigned char* lds, int pool, int blk_lo, int blk_hi) {
;     ...
;         asm volatile("" ::: "memory");
;         cv_finish(cur, lane, scr, v);
;         if (!more) break;
; #pragma unroll
;         for (int i = 0; i < 16; ++i) v[i] = vn[i];
;         cur = nxt; it = nx; }
	v_mul_f32_e32 v4, 0x44000000, v30
	s_waitcnt lgkmcnt(2)
	v_mul_f32_e32 v11, 0x44000000, v32
	v_mov_b32_e32 v3, v129
	v_cvt_pk_fp8_f32 v3, v4, v11
	v_mul_f32_e32 v6, 0x44000000, v26
	v_mul_f32_e32 v8, 0x44000000, v28
	v_cvt_pk_fp8_f32 v2, v6, v8 op_sel:[0,0,1]
	s_waitcnt lgkmcnt(1)
	v_mul_f32_e32 v4, 0x44000000, v34
	s_waitcnt lgkmcnt(0)
	v_mul_f32_e32 v6, 0x44000000, v36
	v_ashrrev_i32_e32 v11, 31, v10
	v_cvt_pk_fp8_f32 v3, v4, v6 op_sel:[0,0,1]
	v_lshlrev_b64 v[10:11], 11, v[10:11]
	v_lshl_add_u64 v[10:11], s[6:7], 0, v[10:11]
	v_lshl_add_u64 v[10:11], v[10:11], 0, s[10:11]
	v_lshl_add_u64 v[10:11], v[10:11], 0, v[130:131]
	global_store_dwordx4 v[10:11], v[0:3], off
	v_mul_f32_e32 v6, 0x44000000, v17
	v_mul_f32_e32 v8, 0x44000000, v33
	v_add_u32_e32 v0, s12, v135
	v_lshlrev_b32_e32 v1, 1, v0
	v_ashrrev_i32_e32 v2, 4, v0
	v_and_b32_e32 v1, 0xf00, v1
	v_and_b32_e32 v2, 0xffffff80, v2
	v_add_u32_e32 v1, v1, v2
	v_and_or_b32 v1, v0, s42, v1
	v_cndmask_b32_e32 v4, v0, v1, vcc
	v_mul_f32_e32 v1, 0x44000000, v5
	v_mul_f32_e32 v2, 0x44000000, v7
	v_mov_b32_e32 v0, v129
	v_cvt_pk_fp8_f32 v0, v1, v2
	v_mul_f32_e32 v2, 0x44000000, v15
	v_mov_b32_e32 v1, v129
	v_cvt_pk_fp8_f32 v1, v2, v6
	v_mul_f32_e32 v3, 0x44000000, v9
	v_mul_f32_e32 v5, 0x44000000, v13
	v_cvt_pk_fp8_f32 v0, v3, v5 op_sel:[0,0,1]
	v_mul_f32_e32 v2, 0x44000000, v19
	v_mul_f32_e32 v3, 0x44000000, v21
	v_cvt_pk_fp8_f32 v1, v2, v3 op_sel:[0,0,1]
	v_mul_f32_e32 v3, 0x44000000, v23
	v_mul_f32_e32 v5, 0x44000000, v25
	v_mov_b32_e32 v2, v129
	v_cvt_pk_fp8_f32 v2, v3, v5
	v_mul_f32_e32 v5, 0x44000000, v31
	v_mov_b32_e32 v3, v129
	v_cvt_pk_fp8_f32 v3, v5, v8
	v_mul_f32_e32 v6, 0x44000000, v27
	v_mul_f32_e32 v7, 0x44000000, v29
	v_cvt_pk_fp8_f32 v2, v6, v7 op_sel:[0,0,1]
	v_mul_f32_e32 v5, 0x44000000, v35
	v_mul_f32_e32 v6, 0x44000000, v37
	v_cvt_pk_fp8_f32 v3, v5, v6 op_sel:[0,0,1]
	v_ashrrev_i32_e32 v5, 31, v4
	v_lshlrev_b64 v[4:5], 11, v[4:5]
	v_lshl_add_u64 v[4:5], s[6:7], 0, v[4:5]
	v_lshl_add_u64 v[4:5], v[4:5], 0, s[10:11]
	v_lshl_add_u64 v[4:5], v[4:5], 0, v[130:131]
	global_store_dwordx4 v[4:5], v[0:3], off
	s_waitcnt lgkmcnt(0)
	s_waitcnt vmcnt(19)
	v_mov_b64_e32 v[4:5], v[56:57]
	s_waitcnt vmcnt(17)
	v_mov_b64_e32 v[12:13], v[72:73]
	v_mov_b64_e32 v[0:1], v[60:61]
	s_waitcnt vmcnt(16)
	v_mov_b64_e32 v[8:9], v[76:77]
	s_waitcnt vmcnt(15)
	v_mov_b64_e32 v[20:21], v[80:81]
	s_waitcnt vmcnt(14)
	v_mov_b64_e32 v[16:17], v[84:85]
	s_waitcnt vmcnt(13)
	v_mov_b64_e32 v[28:29], v[88:89]
	s_waitcnt vmcnt(12)
	v_mov_b64_e32 v[24:25], v[92:93]
	s_waitcnt vmcnt(11)
	v_mov_b64_e32 v[36:37], v[96:97]
	s_waitcnt vmcnt(10)
	v_mov_b64_e32 v[32:33], v[100:101]
	s_waitcnt vmcnt(9)
	v_mov_b64_e32 v[44:45], v[104:105]
	s_waitcnt vmcnt(8)
	v_mov_b64_e32 v[40:41], v[108:109]
	s_waitcnt vmcnt(7)
	v_mov_b64_e32 v[52:53], v[112:113]
	s_waitcnt vmcnt(6)
	v_mov_b64_e32 v[48:49], v[116:117]
	s_waitcnt vmcnt(5)
	v_mov_b64_e32 v[68:69], v[120:121]
	s_waitcnt vmcnt(4)
	v_mov_b64_e32 v[64:65], v[124:125]
	s_andn2_b64 vcc, exec, s[22:23]
	v_mov_b64_e32 v[6:7], v[58:59]
	v_mov_b64_e32 v[2:3], v[62:63]
	v_mov_b64_e32 v[14:15], v[74:75]
	v_mov_b64_e32 v[10:11], v[78:79]
	v_mov_b64_e32 v[22:23], v[82:83]
	v_mov_b64_e32 v[18:19], v[86:87]
	v_mov_b64_e32 v[30:31], v[90:91]
	v_mov_b64_e32 v[26:27], v[94:95]
	v_mov_b64_e32 v[38:39], v[98:99]
	v_mov_b64_e32 v[34:35], v[102:103]
	v_mov_b64_e32 v[46:47], v[106:107]
	v_mov_b64_e32 v[42:43], v[110:111]
	v_mov_b64_e32 v[54:55], v[114:115]
	v_mov_b64_e32 v[50:51], v[118:119]
	v_mov_b64_e32 v[70:71], v[122:123]
	v_mov_b64_e32 v[66:67], v[126:127]
	s_mov_b64 s[6:7], s[16:17]
	s_mov_b32 s11, s14
	s_mov_b32 s10, s45
	s_mov_b32 s12, s38
	s_mov_b32 s38, s44
	s_mov_b32 s14, s43
	s_cbranch_vccz .LBB0_383

; DI CvItem cv_decode(const Params& P, int it) { CvItem c; int item;
;     if (it < NE * CV_GU1) { const int e = it / CV_GU1; c.W = P.in[I_WGU] + (size_t)e * D * 4096; c.N = 4096; c.WT = (unsigned char*)(P.ws + WS_WGU) + (size_t)e * 4096 * D; c.kind = 2; item = it % CV_GU1; }
;     else { const int r = it - NE * CV_GU1; const int e = r / CV_DN1; c.W = P.in[I_WDN] + (size_t)e * D * D; c.N = D; c.WT = (unsigned char*)(P.ws + WS_WDN) + (size_t)e * D * D; c.kind = 3; item = r % CV_DN1; }
;     const int nblk = c.N / 32, kb = item / nblk, nb = item % nblk; c.k0 = 128 * kb; c.n0 = 32 * nb; return c; }
; DI void cv_issue(const CvItem& c, int lane, f32x4 (&v)[16]) { const int c4 = (lane & 7) * 4, r8 = lane >> 3;
; #pragma unroll
;     for (int i = 0; i < 16; ++i) v[i] = *(const f32x4*)(c.W + (size_t)(c.k0 + 8 * i + r8) * c.N + c.n0 + c4); }
; DI void conv_pool(const Params& P, LAS unsigned char* lds, int pool, int blk_lo, int blk_hi) {
;     ...
;     const int blk = claim(); if (blk >= CV_NBLK) return;
;     int it = blk * CV_BLK, left = CV_BLK;
;     CvItem cur = cv_decode(P, it); f32x4 v[16]; cv_issue(cur, lane, v);
.LBB0_1121:
	s_lshr_b32 s13, s16, 5
	s_sext_i32_i16 s2, s10
	v_cvt_f32_ubyte0_e32 v1, s13
	v_cvt_f32_i32_e32 v0, s2
	v_rcp_iflag_f32_e32 v2, v1
	s_mulk_i32 s12, 0x4200
	s_ashr_i32 s2, s2, 30
	s_add_i32 s17, s12, 0
	v_mul_f32_e32 v2, v0, v2
	v_trunc_f32_e32 v2, v2
	v_fma_f32 v0, -v2, v1, v0
	v_cvt_i32_f32_e32 v2, v2
	s_or_b32 s12, s2, 1
	v_cmp_ge_f32_e64 s[2:3], |v0|, v1
	s_and_b64 s[2:3], s[2:3], exec
	s_cselect_b32 s2, s12, 0
	v_readfirstlane_b32 s3, v2
	s_add_i32 s2, s3, s2
	s_sext_i32_i16 s3, s2
	s_mul_i32 s2, s2, s13
	s_sub_i32 s2, s10, s2
	s_sext_i32_i16 s2, s2
	s_lshl_b32 s10, s3, 7
	v_lshlrev_b32_e32 v0, 2, v56
	s_waitcnt vmcnt(15)
	v_ashrrev_i32_e32 v132, 3, v56
	s_lshl_b32 s12, s2, 5
	v_and_b32_e32 v58, 28, v0
	v_add_u32_e32 v0, s10, v132
	v_mad_i64_i32 v[0:1], s[2:3], v0, s16, 0
	s_ashr_i32 s13, s12, 31
	v_lshl_add_u64 v[0:1], v[0:1], 2, s[14:15]
	s_lshl_b64 s[2:3], s[12:13], 2
	s_waitcnt vmcnt(10)
	v_mov_b32_e32 v129, 0
	v_lshl_add_u64 v[0:1], v[0:1], 0, s[2:3]
	v_lshlrev_b32_e32 v128, 2, v58
	v_add_u32_e32 v133, 8, v132
	v_lshl_add_u64 v[8:9], v[0:1], 0, v[128:129]
	v_add_u32_e32 v0, s10, v133
	v_mad_i64_i32 v[0:1], s[18:19], v0, s16, 0
	v_lshl_add_u64 v[0:1], v[0:1], 2, s[14:15]
	v_lshl_add_u64 v[0:1], v[0:1], 0, s[2:3]
	v_add_u32_e32 v134, 16, v132
	v_lshl_add_u64 v[10:11], v[0:1], 0, v[128:129]
	global_load_dwordx4 v[4:7], v[8:9], off nt
	global_load_dwordx4 v[0:3], v[10:11], off nt
	v_add_u32_e32 v8, s10, v134
	v_mad_i64_i32 v[8:9], s[18:19], v8, s16, 0
	v_lshl_add_u64 v[8:9], v[8:9], 2, s[14:15]
	v_lshl_add_u64 v[8:9], v[8:9], 0, s[2:3]
	v_add_u32_e32 v135, 24, v132
	v_lshl_add_u64 v[16:17], v[8:9], 0, v[128:129]
	v_add_u32_e32 v8, s10, v135
	v_mad_i64_i32 v[8:9], s[18:19], v8, s16, 0
	v_lshl_add_u64 v[8:9], v[8:9], 2, s[14:15]
	v_lshl_add_u64 v[8:9], v[8:9], 0, s[2:3]
	v_add_u32_e32 v136, 32, v132
	v_lshl_add_u64 v[18:19], v[8:9], 0, v[128:129]
	global_load_dwordx4 v[12:15], v[16:17], off nt
	global_load_dwordx4 v[8:11], v[18:19], off nt
	v_add_u32_e32 v16, s10, v136
	v_mad_i64_i32 v[16:17], s[18:19], v16, s16, 0
	v_lshl_add_u64 v[16:17], v[16:17], 2, s[14:15]
	v_lshl_add_u64 v[16:17], v[16:17], 0, s[2:3]
	v_add_u32_e32 v137, 40, v132
	v_lshl_add_u64 v[24:25], v[16:17], 0, v[128:129]
	v_add_u32_e32 v16, s10, v137
	v_mad_i64_i32 v[16:17], s[18:19], v16, s16, 0
	v_lshl_add_u64 v[16:17], v[16:17], 2, s[14:15]
	v_lshl_add_u64 v[16:17], v[16:17], 0, s[2:3]
	v_add_u32_e32 v138, 48, v132
	v_lshl_add_u64 v[26:27], v[16:17], 0, v[128:129]
	global_load_dwordx4 v[20:23], v[24:25], off nt
	global_load_dwordx4 v[16:19], v[26:27], off nt
	v_add_u32_e32 v24, s10, v138
	v_mad_i64_i32 v[24:25], s[18:19], v24, s16, 0
	v_lshl_add_u64 v[24:25], v[24:25], 2, s[14:15]
	v_lshl_add_u64 v[24:25], v[24:25], 0, s[2:3]
	v_add_u32_e32 v139, 56, v132
	v_lshl_add_u64 v[32:33], v[24:25], 0, v[128:129]
	v_add_u32_e32 v24, s10, v139
	v_mad_i64_i32 v[24:25], s[18:19], v24, s16, 0
	v_lshl_add_u64 v[24:25], v[24:25], 2, s[14:15]
	v_lshl_add_u64 v[24:25], v[24:25], 0, s[2:3]
	v_add_u32_e32 v140, 64, v132
	v_lshl_add_u64 v[34:35], v[24:25], 0, v[128:129]
	global_load_dwordx4 v[28:31], v[32:33], off nt
	global_load_dwordx4 v[24:27], v[34:35], off nt
	v_add_u32_e32 v32, s10, v140
	v_mad_i64_i32 v[32:33], s[18:19], v32, s16, 0
	v_lshl_add_u64 v[32:33], v[32:33], 2, s[14:15]
	v_lshl_add_u64 v[32:33], v[32:33], 0, s[2:3]
	v_add_u32_e32 v141, 0x48, v132
	v_lshl_add_u64 v[40:41], v[32:33], 0, v[128:129]
	v_add_u32_e32 v32, s10, v141
	v_mad_i64_i32 v[32:33], s[18:19], v32, s16, 0
	v_lshl_add_u64 v[32:33], v[32:33], 2, s[14:15]
	v_lshl_add_u64 v[32:33], v[32:33], 0, s[2:3]
	v_add_u32_e32 v142, 0x50, v132
	v_lshl_add_u64 v[42:43], v[32:33], 0, v[128:129]
	global_load_dwordx4 v[36:39], v[40:41], off nt
	global_load_dwordx4 v[32:35], v[42:43], off nt
	v_add_u32_e32 v40, s10, v142
	v_mad_i64_i32 v[40:41], s[18:19], v40, s16, 0
	v_lshl_add_u64 v[40:41], v[40:41], 2, s[14:15]
	v_lshl_add_u64 v[40:41], v[40:41], 0, s[2:3]
	v_add_u32_e32 v143, 0x58, v132
	v_lshl_add_u64 v[48:49], v[40:41], 0, v[128:129]
	v_add_u32_e32 v40, s10, v143
	v_mad_i64_i32 v[40:41], s[18:19], v40, s16, 0
	v_lshl_add_u64 v[40:41], v[40:41], 2, s[14:15]
	v_lshl_add_u64 v[40:41], v[40:41], 0, s[2:3]
	v_add_u32_e32 v144, 0x60, v132
	v_lshl_add_u64 v[50:51], v[40:41], 0, v[128:129]
	global_load_dwordx4 v[44:47], v[48:49], off nt
	global_load_dwordx4 v[40:43], v[50:51], off nt
	v_add_u32_e32 v48, s10, v144
	v_mad_i64_i32 v[48:49], s[18:19], v48, s16, 0
	v_lshl_add_u64 v[48:49], v[48:49], 2, s[14:15]
	v_lshl_add_u64 v[48:49], v[48:49], 0, s[2:3]
	v_add_u32_e32 v145, 0x68, v132
	s_waitcnt vmcnt(19)
	v_lshl_add_u64 v[60:61], v[48:49], 0, v[128:129]
	v_add_u32_e32 v48, s10, v145
	v_mad_i64_i32 v[48:49], s[18:19], v48, s16, 0
	v_lshl_add_u64 v[48:49], v[48:49], 2, s[14:15]
	v_add_u32_e32 v146, 0x70, v132
	v_lshl_add_u64 v[48:49], v[48:49], 0, s[2:3]
	v_add_u32_e32 v57, s10, v146
	v_add_u32_e32 v147, 0x78, v132
	v_lshl_add_u64 v[62:63], v[48:49], 0, v[128:129]
	global_load_dwordx4 v[52:55], v[60:61], off nt
	global_load_dwordx4 v[48:51], v[62:63], off nt
	v_mad_i64_i32 v[60:61], s[18:19], v57, s16, 0
	v_add_u32_e32 v57, s10, v147
	v_lshl_add_u64 v[60:61], v[60:61], 2, s[14:15]
	v_mad_i64_i32 v[62:63], s[18:19], v57, s16, 0
	v_lshl_add_u64 v[60:61], v[60:61], 0, s[2:3]
	v_lshl_add_u64 v[62:63], v[62:63], 2, s[14:15]
	v_lshl_add_u64 v[60:61], v[60:61], 0, v[128:129]
	v_lshl_add_u64 v[62:63], v[62:63], 0, s[2:3]
	v_lshl_add_u64 v[62:63], v[62:63], 0, v[128:129]
	global_load_dwordx4 v[68:71], v[60:61], off nt
	global_load_dwordx4 v[64:67], v[62:63], off nt
	v_and_b32_e32 v56, 7, v56
	v_lshlrev_b32_e32 v130, 4, v56
	v_mul_u32_u24_e32 v56, 0x840, v56
	v_lshlrev_b32_e32 v60, 2, v132
	v_add_u32_e32 v57, s17, v130
	v_add3_u32 v148, s17, v56, v60
	v_readlane_b32 s16, v254, 2
	v_readlane_b32 s18, v254, 4
	v_readlane_b32 s19, v254, 5
	s_add_u32 s13, s18, 0x12400000
	s_movk_i32 s2, 0x84
	s_addc_u32 s24, s19, 0
	v_mul_lo_u32 v59, v132, s2
	s_add_u32 s25, s18, 0x2400000
	s_mov_b32 s15, 0
	s_mov_b32 s14, 8
	v_mov_b32_e32 v131, v129
	s_addc_u32 s26, s19, 0
	v_lshlrev_b32_e32 v128, 2, v58
	v_add_u32_e32 v149, v57, v59
	s_movk_i32 s27, 0x7f
	v_readlane_b32 s17, v254, 3
	s_branch .LBB0_1124

; #define LAS __attribute__((address_space(3)))
; DI void cv_issue(const CvItem& c, int lane, f32x4 (&v)[16]) { const int c4 = (lane & 7) * 4, r8 = lane >> 3;
; #pragma unroll
;     for (int i = 0; i < 16; ++i) v[i] = *(const f32x4*)(c.W + (size_t)(c.k0 + 8 * i + r8) * c.N + c.n0 + c4); }
; DI void cv_finish(const CvItem& cc, int lane, LAS float* scr, const f32x4 (&v)[16]) {
;     { const int c4 = (lane & 7) * 4, r8 = lane >> 3;
; #pragma unroll
;       for (int i = 0; i < 16; ++i) { LAS float* d = scr + (8 * i + r8) * 33 + c4; d[0] = v[i][0]; d[1] = v[i][1]; d[2] = v[i][2]; d[3] = v[i][3]; } }
; DI void conv_pool(const Params& P, LAS unsigned char* lds, int pool, int blk_lo, int blk_hi) {
;     ...
;     for (;;) { int nx = it + 1; bool more = true;
;     ...
;         const CvItem nxt = cv_decode(P, nx); f32x4 vn[16]; cv_issue(nxt, lane, vn);
.LBB0_1123:
	s_lshr_b32 s21, s34, 5
	s_sext_i32_i16 s2, s20
	v_cvt_f32_ubyte0_e32 v57, s21
	v_cvt_f32_i32_e32 v56, s2
	v_rcp_iflag_f32_e32 v58, v57
	s_ashr_i32 s2, s2, 30
	s_or_b32 s33, s2, 1
	v_mul_f32_e32 v58, v56, v58
	v_trunc_f32_e32 v58, v58
	v_fma_f32 v56, -v58, v57, v56
	v_cvt_i32_f32_e32 v58, v58
	v_cmp_ge_f32_e64 s[2:3], |v56|, v57
	s_and_b64 s[2:3], s[2:3], exec
	s_cselect_b32 s2, s33, 0
	v_readfirstlane_b32 s3, v58
	s_add_i32 s2, s3, s2
	s_sext_i32_i16 s3, s2
	s_mul_i32 s2, s2, s21
	s_sub_i32 s2, s20, s2
	s_sext_i32_i16 s2, s2
	s_lshl_b32 s33, s3, 7
	s_lshl_b32 s20, s2, 5
	v_add_u32_e32 v56, s33, v132
	v_add_u32_e32 v58, s33, v133
	s_waitcnt vmcnt(19)
	v_add_u32_e32 v72, s33, v134
	v_add_u32_e32 v74, s33, v135
	v_add_u32_e32 v80, s33, v136
	v_add_u32_e32 v82, s33, v137
	v_add_u32_e32 v88, s33, v138
	v_add_u32_e32 v90, s33, v139
	s_waitcnt vmcnt(18)
	v_add_u32_e32 v96, s33, v140
	v_add_u32_e32 v98, s33, v141
	v_add_u32_e32 v104, s33, v142
	v_add_u32_e32 v106, s33, v143
	v_add_u32_e32 v112, s33, v144
	v_add_u32_e32 v114, s33, v145
	v_add_u32_e32 v120, s33, v146
	v_add_u32_e32 v122, s33, v147
	v_mad_i64_i32 v[56:57], s[2:3], v56, s34, 0
	s_ashr_i32 s21, s20, 31
	v_mad_i64_i32 v[58:59], s[36:37], v58, s34, 0
	v_mad_i64_i32 v[72:73], s[36:37], v72, s34, 0
	v_mad_i64_i32 v[74:75], s[36:37], v74, s34, 0
	v_mad_i64_i32 v[80:81], s[36:37], v80, s34, 0
	v_mad_i64_i32 v[82:83], s[36:37], v82, s34, 0
	v_mad_i64_i32 v[88:89], s[36:37], v88, s34, 0
	v_mad_i64_i32 v[90:91], s[36:37], v90, s34, 0
	v_mad_i64_i32 v[96:97], s[36:37], v96, s34, 0
	v_mad_i64_i32 v[98:99], s[36:37], v98, s34, 0
	v_mad_i64_i32 v[104:105], s[36:37], v104, s34, 0
	v_mad_i64_i32 v[106:107], s[36:37], v106, s34, 0
	v_mad_i64_i32 v[112:113], s[36:37], v112, s34, 0
	v_mad_i64_i32 v[114:115], s[36:37], v114, s34, 0
	v_mad_i64_i32 v[120:121], s[36:37], v120, s34, 0
	v_mad_i64_i32 v[122:123], s[34:35], v122, s34, 0
	v_lshl_add_u64 v[56:57], v[56:57], 2, s[22:23]
	s_lshl_b64 s[2:3], s[20:21], 2
	v_lshl_add_u64 v[58:59], v[58:59], 2, s[22:23]
	v_lshl_add_u64 v[72:73], v[72:73], 2, s[22:23]
	v_lshl_add_u64 v[74:75], v[74:75], 2, s[22:23]
	v_lshl_add_u64 v[80:81], v[80:81], 2, s[22:23]
	v_lshl_add_u64 v[82:83], v[82:83], 2, s[22:23]
	v_lshl_add_u64 v[88:89], v[88:89], 2, s[22:23]
	v_lshl_add_u64 v[90:91], v[90:91], 2, s[22:23]
	v_lshl_add_u64 v[96:97], v[96:97], 2, s[22:23]
	v_lshl_add_u64 v[98:99], v[98:99], 2, s[22:23]
	v_lshl_add_u64 v[104:105], v[104:105], 2, s[22:23]
	v_lshl_add_u64 v[106:107], v[106:107], 2, s[22:23]
	v_lshl_add_u64 v[112:113], v[112:113], 2, s[22:23]
	v_lshl_add_u64 v[114:115], v[114:115], 2, s[22:23]
	v_lshl_add_u64 v[120:121], v[120:121], 2, s[22:23]
	v_lshl_add_u64 v[122:123], v[122:123], 2, s[22:23]
	v_lshl_add_u64 v[56:57], v[56:57], 0, s[2:3]
	v_lshl_add_u64 v[58:59], v[58:59], 0, s[2:3]
	v_lshl_add_u64 v[72:73], v[72:73], 0, s[2:3]
	v_lshl_add_u64 v[74:75], v[74:75], 0, s[2:3]
	v_lshl_add_u64 v[80:81], v[80:81], 0, s[2:3]
	v_lshl_add_u64 v[82:83], v[82:83], 0, s[2:3]
	v_lshl_add_u64 v[88:89], v[88:89], 0, s[2:3]
	v_lshl_add_u64 v[90:91], v[90:91], 0, s[2:3]
	v_lshl_add_u64 v[96:97], v[96:97], 0, s[2:3]
	v_lshl_add_u64 v[98:99], v[98:99], 0, s[2:3]
	v_lshl_add_u64 v[104:105], v[104:105], 0, s[2:3]
	v_lshl_add_u64 v[106:107], v[106:107], 0, s[2:3]
	v_lshl_add_u64 v[112:113], v[112:113], 0, s[2:3]
	v_lshl_add_u64 v[114:115], v[114:115], 0, s[2:3]
	v_lshl_add_u64 v[120:121], v[120:121], 0, s[2:3]
	v_lshl_add_u64 v[122:123], v[122:123], 0, s[2:3]
	v_lshl_add_u64 v[56:57], v[56:57], 0, v[128:129]
	v_lshl_add_u64 v[60:61], v[58:59], 0, v[128:129]
	v_lshl_add_u64 v[72:73], v[72:73], 0, v[128:129]
	s_waitcnt vmcnt(17)
	v_lshl_add_u64 v[76:77], v[74:75], 0, v[128:129]
	v_lshl_add_u64 v[80:81], v[80:81], 0, v[128:129]
	v_lshl_add_u64 v[84:85], v[82:83], 0, v[128:129]
	v_lshl_add_u64 v[88:89], v[88:89], 0, v[128:129]
	v_lshl_add_u64 v[92:93], v[90:91], 0, v[128:129]
	v_lshl_add_u64 v[96:97], v[96:97], 0, v[128:129]
	v_lshl_add_u64 v[100:101], v[98:99], 0, v[128:129]
	v_lshl_add_u64 v[104:105], v[104:105], 0, v[128:129]
	v_lshl_add_u64 v[108:109], v[106:107], 0, v[128:129]
	v_lshl_add_u64 v[112:113], v[112:113], 0, v[128:129]
	v_lshl_add_u64 v[116:117], v[114:115], 0, v[128:129]
	v_lshl_add_u64 v[120:121], v[120:121], 0, v[128:129]
	v_lshl_add_u64 v[124:125], v[122:123], 0, v[128:129]
	global_load_dwordx4 v[56:59], v[56:57], off nt
	s_nop 0
	global_load_dwordx4 v[60:63], v[60:61], off nt
	s_nop 0
	global_load_dwordx4 v[72:75], v[72:73], off nt
	s_nop 0
	global_load_dwordx4 v[76:79], v[76:77], off nt
	s_nop 0
	global_load_dwordx4 v[80:83], v[80:81], off nt
	s_nop 0
	global_load_dwordx4 v[84:87], v[84:85], off nt
	s_nop 0
	global_load_dwordx4 v[88:91], v[88:89], off nt
	s_nop 0
	global_load_dwordx4 v[92:95], v[92:93], off nt
	s_nop 0
	global_load_dwordx4 v[96:99], v[96:97], off nt
	s_nop 0
	global_load_dwordx4 v[100:103], v[100:101], off nt
	s_nop 0
	global_load_dwordx4 v[104:107], v[104:105], off nt
	s_nop 0
	global_load_dwordx4 v[108:111], v[108:109], off nt
	s_nop 0
	global_load_dwordx4 v[112:115], v[112:113], off nt
	s_nop 0
	global_load_dwordx4 v[116:119], v[116:117], off nt
	s_nop 0
	global_load_dwordx4 v[120:123], v[120:121], off nt
	s_nop 0
	global_load_dwordx4 v[124:127], v[124:125], off nt
	s_waitcnt vmcnt(31)
	ds_write2_b32 v149, v4, v5 offset1:1
	ds_write2_b32 v149, v6, v7 offset0:2 offset1:3
	v_add_u32_e32 v4, 0x420, v149
	s_waitcnt vmcnt(30)
	ds_write2_b32 v4, v0, v1 offset1:1
	v_add_u32_e32 v0, 0x428, v149
	ds_write2_b32 v0, v2, v3 offset1:1
	v_add_u32_e32 v0, 0x840, v149
	s_waitcnt vmcnt(29)
; #define LAS __attribute__((address_space(3)))
; DI unsigned pk4f8(float a, float b, float c, float d) { int p = __builtin_amdgcn_cvt_pk_fp8_f32(a, b, 0, false); p = __builtin_amdgcn_cvt_pk_fp8_f32(c, d, p, true); return (unsigned)p; }
; DI void cv_finish(const CvItem& cc, int lane, LAS float* scr, const f32x4 (&v)[16]) {
;     { const int c4 = (lane & 7) * 4, r8 = lane >> 3;
; #pragma unroll
;       for (int i = 0; i < 16; ++i) { LAS float* d = scr + (8 * i + r8) * 33 + c4; d[0] = v[i][0]; d[1] = v[i][1]; d[2] = v[i][2]; d[3] = v[i][3]; } }
;     asm volatile("s_waitcnt lgkmcnt(0)" ::: "memory");
;     const int c = lane & 7;
; #pragma unroll
;     for (int j = 0; j < 4; ++j) { const int n = (lane >> 3) + 8 * j; const int src = cc.n0 + n; int dst = src;
;         if (cc.kind == 2) { const int jj = src & 2047; dst = (jj >> 7) * 256 + (src >> 11) * 128 + (jj & 127); }
;         const LAS float* sp = scr + (16 * c) * 33 + n;
;         u32x4 o; o.x = pk4f8(sp[0 * 33] * WSCALE, sp[1 * 33] * WSCALE, sp[2 * 33] * WSCALE, sp[3 * 33] * WSCALE); o.y = pk4f8(sp[4 * 33] * WSCALE, sp[5 * 33] * WSCALE, sp[6 * 33] * WSCALE, sp[7 * 33] * WSCALE);
;         o.z = pk4f8(sp[8 * 33] * WSCALE, sp[9 * 33] * WSCALE, sp[10 * 33] * WSCALE, sp[11 * 33] * WSCALE); o.w = pk4f8(sp[12 * 33] * WSCALE, sp[13 * 33] * WSCALE, sp[14 * 33] * WSCALE, sp[15 * 33] * WSCALE);
;         *(u32x4*)(cc.WT + (size_t)dst * D + cc.k0 + 16 * c) = o; }
	ds_write2_b32 v0, v12, v13 offset1:1
	v_add_u32_e32 v0, 0x848, v149
	ds_write2_b32 v0, v14, v15 offset1:1
	v_add_u32_e32 v0, 0xc60, v149
	s_waitcnt vmcnt(28)
	ds_write2_b32 v0, v8, v9 offset1:1
	v_add_u32_e32 v0, 0xc68, v149
	ds_write2_b32 v0, v10, v11 offset1:1
	v_add_u32_e32 v0, 0x1080, v149
	s_waitcnt vmcnt(27)
	ds_write2_b32 v0, v20, v21 offset1:1
	v_add_u32_e32 v0, 0x1088, v149
	ds_write2_b32 v0, v22, v23 offset1:1
	v_add_u32_e32 v0, 0x14a0, v149
	s_waitcnt vmcnt(26)
	ds_write2_b32 v0, v16, v17 offset1:1
	v_add_u32_e32 v0, 0x14a8, v149
	ds_write2_b32 v0, v18, v19 offset1:1
	v_add_u32_e32 v0, 0x18c0, v149
	s_waitcnt vmcnt(25)
	ds_write2_b32 v0, v28, v29 offset1:1
	v_add_u32_e32 v0, 0x18c8, v149
	ds_write2_b32 v0, v30, v31 offset1:1
	v_add_u32_e32 v0, 0x1ce0, v149
	s_waitcnt vmcnt(24)
	ds_write2_b32 v0, v24, v25 offset1:1
	v_add_u32_e32 v0, 0x1ce8, v149
	ds_write2_b32 v0, v26, v27 offset1:1
	v_add_u32_e32 v0, 0x2100, v149
	s_waitcnt vmcnt(23)
	ds_write2_b32 v0, v36, v37 offset1:1
	v_add_u32_e32 v0, 0x2108, v149
	ds_write2_b32 v0, v38, v39 offset1:1
	v_add_u32_e32 v0, 0x2520, v149
	s_waitcnt vmcnt(22)
	ds_write2_b32 v0, v32, v33 offset1:1
	v_add_u32_e32 v0, 0x2528, v149
	ds_write2_b32 v0, v34, v35 offset1:1
	v_add_u32_e32 v0, 0x2940, v149
	s_waitcnt vmcnt(21)
	ds_write2_b32 v0, v44, v45 offset1:1
	v_add_u32_e32 v0, 0x2948, v149
	ds_write2_b32 v0, v46, v47 offset1:1
	v_add_u32_e32 v0, 0x2d60, v149
	s_waitcnt vmcnt(20)
	ds_write2_b32 v0, v40, v41 offset1:1
	v_add_u32_e32 v0, 0x2d68, v149
	ds_write2_b32 v0, v42, v43 offset1:1
	v_add_u32_e32 v0, 0x3180, v149
	s_waitcnt vmcnt(19)
	ds_write2_b32 v0, v52, v53 offset1:1
	v_add_u32_e32 v0, 0x3188, v149
	ds_write2_b32 v0, v54, v55 offset1:1
	v_add_u32_e32 v0, 0x35a0, v149
	s_waitcnt vmcnt(18)
	ds_write2_b32 v0, v48, v49 offset1:1
	v_add_u32_e32 v0, 0x35a8, v149
	ds_write2_b32 v0, v50, v51 offset1:1
	v_add_u32_e32 v0, 0x39c0, v149
	s_waitcnt vmcnt(17)
	ds_write2_b32 v0, v68, v69 offset1:1
	v_add_u32_e32 v0, 0x39c8, v149
	ds_write2_b32 v0, v70, v71 offset1:1
	v_add_u32_e32 v0, 0x3de0, v149
	s_waitcnt vmcnt(16)
	ds_write2_b32 v0, v64, v65 offset1:1
	v_add_u32_e32 v0, 0x3de8, v149
	ds_write2_b32 v0, v66, v67 offset1:1
	s_waitcnt lgkmcnt(0)
	v_add_u32_e32 v0, s12, v132
	v_lshlrev_b32_e32 v1, 1, v0
	v_ashrrev_i32_e32 v2, 4, v0
	ds_read2_b32 v[4:5], v148 offset1:8
	ds_read2_b32 v[6:7], v148 offset0:33 offset1:41
	ds_read2_b32 v[8:9], v148 offset0:66 offset1:74
	v_and_b32_e32 v1, 0xf00, v1
	v_and_b32_e32 v2, 0xffffff80, v2
	s_cmp_eq_u32 s11, 2
	v_add_u32_e32 v1, v1, v2
	v_and_or_b32 v1, v0, s27, v1
	s_cselect_b64 vcc, -1, 0
	ds_read2_b32 v[12:13], v148 offset0:99 offset1:107
	v_cndmask_b32_e32 v10, v0, v1, vcc
	s_waitcnt lgkmcnt(3)
	v_mul_f32_e32 v1, 0x44000000, v4
	s_waitcnt lgkmcnt(2)
	v_mul_f32_e32 v2, 0x44000000, v6
	v_mov_b32_e32 v0, v129
	v_cvt_pk_fp8_f32 v0, v1, v2
	ds_read2_b32 v[14:15], v148 offset0:132 offset1:140
	ds_read2_b32 v[16:17], v148 offset0:165 offset1:173
	ds_read2_b32 v[18:19], v148 offset0:198 offset1:206
	s_waitcnt lgkmcnt(4)
	v_mul_f32_e32 v3, 0x44000000, v8
	s_waitcnt lgkmcnt(3)
	v_mul_f32_e32 v1, 0x44000000, v12
	ds_read2_b32 v[20:21], v148 offset0:231 offset1:239
	v_add_u32_e32 v38, 0x400, v148
	v_cvt_pk_fp8_f32 v0, v3, v1 op_sel:[0,0,1]
	s_waitcnt lgkmcnt(3)
	v_mul_f32_e32 v2, 0x44000000, v14
	s_waitcnt lgkmcnt(2)
	v_mul_f32_e32 v3, 0x44000000, v16
	v_mov_b32_e32 v1, v129
	ds_read2_b32 v[22:23], v38 offset0:8 offset1:16
	v_cvt_pk_fp8_f32 v1, v2, v3
	ds_read2_b32 v[24:25], v38 offset0:41 offset1:49
	ds_read2_b32 v[26:27], v38 offset0:74 offset1:82
	ds_read2_b32 v[28:29], v38 offset0:107 offset1:115
	ds_read2_b32 v[30:31], v38 offset0:140 offset1:148
	ds_read2_b32 v[32:33], v38 offset0:173 offset1:181
	s_waitcnt lgkmcnt(7)
	v_mul_f32_e32 v4, 0x44000000, v18
	s_waitcnt lgkmcnt(6)
	v_mul_f32_e32 v2, 0x44000000, v20
	v_cvt_pk_fp8_f32 v1, v4, v2 op_sel:[0,0,1]
	s_waitcnt lgkmcnt(5)
	v_mul_f32_e32 v3, 0x44000000, v22
	s_waitcnt lgkmcnt(4)
	v_mul_f32_e32 v4, 0x44000000, v24
	v_mov_b32_e32 v2, v129
	ds_read2_b32 v[34:35], v38 offset0:206 offset1:214
	ds_read2_b32 v[36:37], v38 offset0:239 offset1:247
	v_cvt_pk_fp8_f32 v2, v3, v4
	s_waitcnt lgkmcnt(3)
	v_mul_f32_e32 v4, 0x44000000, v30
	s_waitcnt lgkmcnt(2)
	v_mul_f32_e32 v11, 0x44000000, v32
	v_mov_b32_e32 v3, v129
	v_cvt_pk_fp8_f32 v3, v4, v11
	v_mul_f32_e32 v6, 0x44000000, v26
	v_mul_f32_e32 v8, 0x44000000, v28
	v_cvt_pk_fp8_f32 v2, v6, v8 op_sel:[0,0,1]
	s_waitcnt lgkmcnt(1)
	v_mul_f32_e32 v4, 0x44000000, v34
	s_waitcnt lgkmcnt(0)
; #define LAS __attribute__((address_space(3)))
; DI unsigned pk4f8(float a, float b, float c, float d) { int p = __builtin_amdgcn_cvt_pk_fp8_f32(a, b, 0, false); p = __builtin_amdgcn_cvt_pk_fp8_f32(c, d, p, true); return (unsigned)p; }
; DI void cv_finish(const CvItem& cc, int lane, LAS float* scr, const f32x4 (&v)[16]) {
;     ...
;     const int c = lane & 7;
; #pragma unroll
;     for (int j = 0; j < 4; ++j) { const int n = (lane >> 3) + 8 * j; const int src = cc.n0 + n; int dst = src;
;         if (cc.kind == 2) { const int jj = src & 2047; dst = (jj >> 7) * 256 + (src >> 11) * 128 + (jj & 127); }
;         const LAS float* sp = scr + (16 * c) * 33 + n;
;         u32x4 o; o.x = pk4f8(sp[0 * 33] * WSCALE, sp[1 * 33] * WSCALE, sp[2 * 33] * WSCALE, sp[3 * 33] * WSCALE); o.y = pk4f8(sp[4 * 33] * WSCALE, sp[5 * 33] * WSCALE, sp[6 * 33] * WSCALE, sp[7 * 33] * WSCALE);
;         o.z = pk4f8(sp[8 * 33] * WSCALE, sp[9 * 33] * WSCALE, sp[10 * 33] * WSCALE, sp[11 * 33] * WSCALE); o.w = pk4f8(sp[12 * 33] * WSCALE, sp[13 * 33] * WSCALE, sp[14 * 33] * WSCALE, sp[15 * 33] * WSCALE);
;         *(u32x4*)(cc.WT + (size_t)dst * D + cc.k0 + 16 * c) = o; }
	v_mul_f32_e32 v6, 0x44000000, v36
	v_ashrrev_i32_e32 v11, 31, v10
	v_cvt_pk_fp8_f32 v3, v4, v6 op_sel:[0,0,1]
	v_lshlrev_b64 v[10:11], 11, v[10:11]
	v_lshl_add_u64 v[10:11], s[6:7], 0, v[10:11]
	s_ashr_i32 s11, s10, 31
	v_lshl_add_u64 v[10:11], v[10:11], 0, s[10:11]
	v_lshl_add_u64 v[10:11], v[10:11], 0, v[130:131]
	global_store_dwordx4 v[10:11], v[0:3], off
	v_mul_f32_e32 v6, 0x44000000, v17
	v_mul_f32_e32 v8, 0x44000000, v33
	v_add_u32_e32 v0, s12, v133
	v_lshlrev_b32_e32 v1, 1, v0
	v_ashrrev_i32_e32 v2, 4, v0
	v_and_b32_e32 v1, 0xf00, v1
	v_and_b32_e32 v2, 0xffffff80, v2
	v_add_u32_e32 v1, v1, v2
	v_and_or_b32 v1, v0, s27, v1
	v_cndmask_b32_e32 v4, v0, v1, vcc
	v_mul_f32_e32 v1, 0x44000000, v5
	v_mul_f32_e32 v2, 0x44000000, v7
	v_mov_b32_e32 v0, v129
	v_cvt_pk_fp8_f32 v0, v1, v2
	v_mul_f32_e32 v2, 0x44000000, v15
	v_mov_b32_e32 v1, v129
	v_cvt_pk_fp8_f32 v1, v2, v6
	v_mul_f32_e32 v3, 0x44000000, v9
	v_mul_f32_e32 v5, 0x44000000, v13
	v_cvt_pk_fp8_f32 v0, v3, v5 op_sel:[0,0,1]
	v_mul_f32_e32 v2, 0x44000000, v19
	v_mul_f32_e32 v3, 0x44000000, v21
	v_cvt_pk_fp8_f32 v1, v2, v3 op_sel:[0,0,1]
	v_mul_f32_e32 v3, 0x44000000, v23
	v_mul_f32_e32 v5, 0x44000000, v25
	v_mov_b32_e32 v2, v129
	v_cvt_pk_fp8_f32 v2, v3, v5
	v_mul_f32_e32 v5, 0x44000000, v31
	v_mov_b32_e32 v3, v129
	v_cvt_pk_fp8_f32 v3, v5, v8
	v_mul_f32_e32 v6, 0x44000000, v27
	v_mul_f32_e32 v7, 0x44000000, v29
	v_cvt_pk_fp8_f32 v2, v6, v7 op_sel:[0,0,1]
	v_mul_f32_e32 v5, 0x44000000, v35
	v_mul_f32_e32 v6, 0x44000000, v37
	v_cvt_pk_fp8_f32 v3, v5, v6 op_sel:[0,0,1]
	v_ashrrev_i32_e32 v5, 31, v4
	v_lshlrev_b64 v[4:5], 11, v[4:5]
	v_lshl_add_u64 v[4:5], s[6:7], 0, v[4:5]
	v_lshl_add_u64 v[4:5], v[4:5], 0, s[10:11]
	v_lshl_add_u64 v[4:5], v[4:5], 0, v[130:131]
	global_store_dwordx4 v[4:5], v[0:3], off
	ds_read2_b32 v[4:5], v148 offset0:16 offset1:24
	ds_read2_b32 v[6:7], v148 offset0:49 offset1:57
	ds_read2_b32 v[8:9], v148 offset0:82 offset1:90
	v_add_u32_e32 v0, s12, v134
	v_lshlrev_b32_e32 v1, 1, v0
	v_ashrrev_i32_e32 v2, 4, v0
	v_and_b32_e32 v1, 0xf00, v1
	v_and_b32_e32 v2, 0xffffff80, v2
	v_add_u32_e32 v1, v1, v2
	v_and_or_b32 v1, v0, s27, v1
	ds_read2_b32 v[12:13], v148 offset0:115 offset1:123
	v_cndmask_b32_e32 v10, v0, v1, vcc
	s_waitcnt lgkmcnt(3)
	v_mul_f32_e32 v1, 0x44000000, v4
	s_waitcnt lgkmcnt(2)
	v_mul_f32_e32 v2, 0x44000000, v6
	v_mov_b32_e32 v0, v129
	ds_read2_b32 v[14:15], v148 offset0:148 offset1:156
	ds_read2_b32 v[16:17], v148 offset0:181 offset1:189
	v_cvt_pk_fp8_f32 v0, v1, v2
	s_waitcnt lgkmcnt(3)
	v_mul_f32_e32 v3, 0x44000000, v8
	s_waitcnt lgkmcnt(2)
	v_mul_f32_e32 v1, 0x44000000, v12
	ds_read2_b32 v[18:19], v148 offset0:214 offset1:222
	ds_read2_b32 v[20:21], v148 offset0:247 offset1:255
	v_cvt_pk_fp8_f32 v0, v3, v1 op_sel:[0,0,1]
	s_waitcnt lgkmcnt(3)
	v_mul_f32_e32 v2, 0x44000000, v14
	s_waitcnt lgkmcnt(2)
	v_mul_f32_e32 v3, 0x44000000, v16
	v_mov_b32_e32 v1, v129
	ds_read2_b32 v[22:23], v38 offset0:24 offset1:32
	v_cvt_pk_fp8_f32 v1, v2, v3
	ds_read2_b32 v[24:25], v38 offset0:57 offset1:65
	ds_read2_b32 v[26:27], v38 offset0:90 offset1:98
	ds_read2_b32 v[28:29], v38 offset0:123 offset1:131
	ds_read2_b32 v[30:31], v38 offset0:156 offset1:164
	ds_read2_b32 v[32:33], v38 offset0:189 offset1:197
	s_waitcnt lgkmcnt(7)
	v_mul_f32_e32 v4, 0x44000000, v18
	s_waitcnt lgkmcnt(6)
	v_mul_f32_e32 v2, 0x44000000, v20
	v_cvt_pk_fp8_f32 v1, v4, v2 op_sel:[0,0,1]
	s_waitcnt lgkmcnt(5)
	v_mul_f32_e32 v3, 0x44000000, v22
	s_waitcnt lgkmcnt(4)
	v_mul_f32_e32 v4, 0x44000000, v24
	v_mov_b32_e32 v2, v129
	v_cvt_pk_fp8_f32 v2, v3, v4
	v_add_u32_e32 v3, 0x600, v148
	ds_read2_b32 v[34:35], v38 offset0:222 offset1:230
	ds_read2_b32 v[36:37], v3 offset0:127 offset1:135
	s_waitcnt lgkmcnt(3)
; #define LAS __attribute__((address_space(3)))
; DI unsigned pk4f8(float a, float b, float c, float d) { int p = __builtin_amdgcn_cvt_pk_fp8_f32(a, b, 0, false); p = __builtin_amdgcn_cvt_pk_fp8_f32(c, d, p, true); return (unsigned)p; }
; DI void cv_finish(const CvItem& cc, int lane, LAS float* scr, const f32x4 (&v)[16]) {
;     ...
;     for (int j = 0; j < 4; ++j) { const int n = (lane >> 3) + 8 * j; const int src = cc.n0 + n; int dst = src;
;         if (cc.kind == 2) { const int jj = src & 2047; dst = (jj >> 7) * 256 + (src >> 11) * 128 + (jj & 127); }
;         const LAS float* sp = scr + (16 * c) * 33 + n;
;         u32x4 o; o.x = pk4f8(sp[0 * 33] * WSCALE, sp[1 * 33] * WSCALE, sp[2 * 33] * WSCALE, sp[3 * 33] * WSCALE); o.y = pk4f8(sp[4 * 33] * WSCALE, sp[5 * 33] * WSCALE, sp[6 * 33] * WSCALE, sp[7 * 33] * WSCALE);
;         o.z = pk4f8(sp[8 * 33] * WSCALE, sp[9 * 33] * WSCALE, sp[10 * 33] * WSCALE, sp[11 * 33] * WSCALE); o.w = pk4f8(sp[12 * 33] * WSCALE, sp[13 * 33] * WSCALE, sp[14 * 33] * WSCALE, sp[15 * 33] * WSCALE);
;         *(u32x4*)(cc.WT + (size_t)dst * D + cc.k0 + 16 * c) = o; }
; DI void conv_pool(const Params& P, LAS unsigned char* lds, int pool, int blk_lo, int blk_hi) {
;     ...
;         if (!more) break;
; #pragma unroll
;         for (int i = 0; i < 16; ++i) v[i] = vn[i];
;         cur = nxt; it = nx; }
	v_mul_f32_e32 v4, 0x44000000, v30
	s_waitcnt lgkmcnt(2)
	v_mul_f32_e32 v11, 0x44000000, v32
	v_mov_b32_e32 v3, v129
	v_cvt_pk_fp8_f32 v3, v4, v11
	v_mul_f32_e32 v6, 0x44000000, v26
	v_mul_f32_e32 v8, 0x44000000, v28
	v_cvt_pk_fp8_f32 v2, v6, v8 op_sel:[0,0,1]
	s_waitcnt lgkmcnt(1)
	v_mul_f32_e32 v4, 0x44000000, v34
	s_waitcnt lgkmcnt(0)
	v_mul_f32_e32 v6, 0x44000000, v36
	v_ashrrev_i32_e32 v11, 31, v10
	v_cvt_pk_fp8_f32 v3, v4, v6 op_sel:[0,0,1]
	v_lshlrev_b64 v[10:11], 11, v[10:11]
	v_lshl_add_u64 v[10:11], s[6:7], 0, v[10:11]
	v_lshl_add_u64 v[10:11], v[10:11], 0, s[10:11]
	v_lshl_add_u64 v[10:11], v[10:11], 0, v[130:131]
	global_store_dwordx4 v[10:11], v[0:3], off
	v_mul_f32_e32 v6, 0x44000000, v17
	v_mul_f32_e32 v8, 0x44000000, v33
	v_add_u32_e32 v0, s12, v135
	v_lshlrev_b32_e32 v1, 1, v0
	v_ashrrev_i32_e32 v2, 4, v0
	v_and_b32_e32 v1, 0xf00, v1
	v_and_b32_e32 v2, 0xffffff80, v2
	v_add_u32_e32 v1, v1, v2
	v_and_or_b32 v1, v0, s27, v1
	v_cndmask_b32_e32 v4, v0, v1, vcc
	v_mul_f32_e32 v1, 0x44000000, v5
	v_mul_f32_e32 v2, 0x44000000, v7
	v_mov_b32_e32 v0, v129
	v_cvt_pk_fp8_f32 v0, v1, v2
	v_mul_f32_e32 v2, 0x44000000, v15
	v_mov_b32_e32 v1, v129
	v_cvt_pk_fp8_f32 v1, v2, v6
	v_mul_f32_e32 v3, 0x44000000, v9
	v_mul_f32_e32 v5, 0x44000000, v13
	v_cvt_pk_fp8_f32 v0, v3, v5 op_sel:[0,0,1]
	v_mul_f32_e32 v2, 0x44000000, v19
	v_mul_f32_e32 v3, 0x44000000, v21
	v_cvt_pk_fp8_f32 v1, v2, v3 op_sel:[0,0,1]
	v_mul_f32_e32 v3, 0x44000000, v23
	v_mul_f32_e32 v5, 0x44000000, v25
	v_mov_b32_e32 v2, v129
	v_cvt_pk_fp8_f32 v2, v3, v5
	v_mul_f32_e32 v5, 0x44000000, v31
	v_mov_b32_e32 v3, v129
	v_cvt_pk_fp8_f32 v3, v5, v8
	v_mul_f32_e32 v6, 0x44000000, v27
	v_mul_f32_e32 v7, 0x44000000, v29
	v_cvt_pk_fp8_f32 v2, v6, v7 op_sel:[0,0,1]
	v_mul_f32_e32 v5, 0x44000000, v35
	v_mul_f32_e32 v6, 0x44000000, v37
	v_cvt_pk_fp8_f32 v3, v5, v6 op_sel:[0,0,1]
	v_ashrrev_i32_e32 v5, 31, v4
	v_lshlrev_b64 v[4:5], 11, v[4:5]
	v_lshl_add_u64 v[4:5], s[6:7], 0, v[4:5]
	v_lshl_add_u64 v[4:5], v[4:5], 0, s[10:11]
	v_lshl_add_u64 v[4:5], v[4:5], 0, v[130:131]
	global_store_dwordx4 v[4:5], v[0:3], off
	s_waitcnt lgkmcnt(0)
	s_waitcnt vmcnt(19)
	v_mov_b64_e32 v[4:5], v[56:57]
	s_waitcnt vmcnt(17)
	v_mov_b64_e32 v[12:13], v[72:73]
	v_mov_b64_e32 v[0:1], v[60:61]
	s_waitcnt vmcnt(16)
	v_mov_b64_e32 v[8:9], v[76:77]
	s_waitcnt vmcnt(15)
	v_mov_b64_e32 v[20:21], v[80:81]
	s_waitcnt vmcnt(14)
	v_mov_b64_e32 v[16:17], v[84:85]
	s_waitcnt vmcnt(13)
	v_mov_b64_e32 v[28:29], v[88:89]
	s_waitcnt vmcnt(12)
	v_mov_b64_e32 v[24:25], v[92:93]
	s_waitcnt vmcnt(11)
	v_mov_b64_e32 v[36:37], v[96:97]
	s_waitcnt vmcnt(10)
	v_mov_b64_e32 v[32:33], v[100:101]
	s_waitcnt vmcnt(9)
	v_mov_b64_e32 v[44:45], v[104:105]
	s_waitcnt vmcnt(8)
	v_mov_b64_e32 v[40:41], v[108:109]
	s_waitcnt vmcnt(7)
	v_mov_b64_e32 v[52:53], v[112:113]
	s_waitcnt vmcnt(6)
	v_mov_b64_e32 v[48:49], v[116:117]
	s_waitcnt vmcnt(5)
	v_mov_b64_e32 v[68:69], v[120:121]
	s_waitcnt vmcnt(4)
	v_mov_b64_e32 v[64:65], v[124:125]
	s_andn2_b64 vcc, exec, s[18:19]
	v_mov_b64_e32 v[6:7], v[58:59]
	v_mov_b64_e32 v[2:3], v[62:63]
	v_mov_b64_e32 v[14:15], v[74:75]
	v_mov_b64_e32 v[10:11], v[78:79]
	v_mov_b64_e32 v[22:23], v[82:83]
	v_mov_b64_e32 v[18:19], v[86:87]
	v_mov_b64_e32 v[30:31], v[90:91]
	v_mov_b64_e32 v[26:27], v[94:95]
	v_mov_b64_e32 v[38:39], v[98:99]
	v_mov_b64_e32 v[34:35], v[102:103]
	v_mov_b64_e32 v[46:47], v[106:107]
	v_mov_b64_e32 v[42:43], v[110:111]
	v_mov_b64_e32 v[54:55], v[114:115]
	v_mov_b64_e32 v[50:51], v[118:119]
	v_mov_b64_e32 v[70:71], v[122:123]
	v_mov_b64_e32 v[66:67], v[126:127]
	s_mov_b64 s[6:7], s[16:17]
	s_mov_b32 s11, s14
	s_mov_b32 s10, s33
	s_mov_b32 s12, s20
	s_mov_b32 s20, s29
	s_mov_b32 s14, s28
	s_cbranch_vccz .LBB0_1136
